# speedup vs baseline: 1.0161x; 1.0080x over previous
.LBB1_10:
	s_or_b64 exec, exec, s[4:5]
	ds_read_b128 v[198:201], v177 offset:224
	ds_read_b128 v[202:205], v177 offset:192
	ds_read_b128 v[206:209], v177 offset:160
	ds_read_b128 v[210:213], v177 offset:128
.LBB1_11:
	v_fma_f32 v4, -v1, v16, -v178
	v_mul_f32_e32 v4, 0x3e0293ee, v4
	v_fmamk_f32 v6, v98, 0x3e0293ee, v4
	v_fmamk_f32 v7, v99, 0x3e0293ee, v4
	v_fmamk_f32 v8, v100, 0x3e0293ee, v4
	v_fmamk_f32 v9, v101, 0x3e0293ee, v4
	v_fmamk_f32 v10, v102, 0x3e0293ee, v4
	v_fmamk_f32 v11, v103, 0x3e0293ee, v4
	v_fmamk_f32 v12, v104, 0x3e0293ee, v4
	v_fmamk_f32 v13, v105, 0x3e0293ee, v4
	v_fmamk_f32 v14, v106, 0x3e0293ee, v4
	v_fmamk_f32 v15, v107, 0x3e0293ee, v4
	v_fmamk_f32 v16, v108, 0x3e0293ee, v4
	v_fmamk_f32 v17, v109, 0x3e0293ee, v4
	v_fmamk_f32 v98, v110, 0x3e0293ee, v4
	v_fmamk_f32 v99, v111, 0x3e0293ee, v4
	v_fmamk_f32 v100, v112, 0x3e0293ee, v4
	v_fmamk_f32 v101, v113, 0x3e0293ee, v4
	s_add_u32 s76, s76, 0x10000
	v_exp_f32_e32 v190, v6
	v_exp_f32_e32 v191, v7
	v_exp_f32_e32 v188, v8
	v_exp_f32_e32 v189, v9
	v_exp_f32_e32 v186, v10
	v_exp_f32_e32 v187, v11
	v_exp_f32_e32 v184, v12
	v_exp_f32_e32 v185, v13
	v_exp_f32_e32 v182, v14
	v_exp_f32_e32 v183, v15
	v_exp_f32_e32 v156, v16
	v_exp_f32_e32 v157, v17
	v_exp_f32_e32 v148, v98
	v_exp_f32_e32 v149, v99
	v_exp_f32_e32 v146, v100
	v_exp_f32_e32 v147, v101
	s_addc_u32 s77, s77, 0
	s_addk_i32 s68, 0x100
	v_add_f32_e32 v3, v3, v180
	s_add_u32 s74, s74, 0x10000
	v_fmac_f32_e32 v3, v170, v166
	v_add_f32_e32 v166, v192, v193
	s_addc_u32 s75, s75, 0
	v_pk_fma_f32 v[112:113], v[96:97], s[94:95], v[4:5] op_sel_hi:[1,0,0]
	v_pk_fma_f32 v[110:111], v[94:95], s[94:95], v[4:5] op_sel_hi:[1,0,0]
	v_pk_fma_f32 v[108:109], v[92:93], s[94:95], v[4:5] op_sel_hi:[1,0,0]
	v_pk_fma_f32 v[106:107], v[90:91], s[94:95], v[4:5] op_sel_hi:[1,0,0]
	v_pk_fma_f32 v[104:105], v[88:89], s[94:95], v[4:5] op_sel_hi:[1,0,0]
	v_pk_fma_f32 v[102:103], v[86:87], s[94:95], v[4:5] op_sel_hi:[1,0,0]
	v_pk_fma_f32 v[100:101], v[84:85], s[94:95], v[4:5] op_sel_hi:[1,0,0]
	v_pk_fma_f32 v[98:99], v[82:83], s[94:95], v[4:5] op_sel_hi:[1,0,0]
	v_fmac_f32_e32 v166, v3, v181
	s_cmp_lt_u32 s72, s83
	v_add_u32_e32 v179, 0xffffff00, v179
	v_mov_b32_e32 v170, v5
	s_cbranch_vccz .Lnoresc2
	s_waitcnt lgkmcnt(0)
	v_pk_mul_f32 v[64:65], v[64:65], v[200:201]
	v_pk_mul_f32 v[60:61], v[60:61], v[204:205]
	v_pk_mul_f32 v[56:57], v[56:57], v[208:209]
	v_pk_mul_f32 v[52:53], v[52:53], v[212:213]
	v_pk_mul_f32 v[62:63], v[62:63], v[198:199]
	v_pk_mul_f32 v[58:59], v[58:59], v[202:203]
	v_pk_mul_f32 v[54:55], v[54:55], v[206:207]
	v_pk_mul_f32 v[50:51], v[50:51], v[210:211]
	v_pk_mul_f32 v[32:33], v[32:33], v[200:201]
	v_pk_mul_f32 v[28:29], v[28:29], v[204:205]
	v_pk_mul_f32 v[24:25], v[24:25], v[208:209]
	v_pk_mul_f32 v[20:21], v[20:21], v[212:213]
	v_pk_mul_f32 v[30:31], v[30:31], v[198:199]
	v_pk_mul_f32 v[26:27], v[26:27], v[202:203]
	v_pk_mul_f32 v[22:23], v[22:23], v[206:207]
	v_pk_mul_f32 v[18:19], v[18:19], v[210:211]
	v_pk_mul_f32 v[80:81], v[80:81], v[200:201]
	v_pk_mul_f32 v[76:77], v[76:77], v[204:205]
	v_pk_mul_f32 v[72:73], v[72:73], v[208:209]
	v_pk_mul_f32 v[68:69], v[68:69], v[212:213]
	v_pk_mul_f32 v[78:79], v[78:79], v[198:199]
	v_pk_mul_f32 v[74:75], v[74:75], v[202:203]
	v_pk_mul_f32 v[70:71], v[70:71], v[206:207]
	v_pk_mul_f32 v[66:67], v[66:67], v[210:211]
	v_pk_mul_f32 v[48:49], v[48:49], v[200:201]
	v_pk_mul_f32 v[44:45], v[44:45], v[204:205]
	v_pk_mul_f32 v[40:41], v[40:41], v[208:209]
	v_pk_mul_f32 v[36:37], v[36:37], v[212:213]
	v_pk_mul_f32 v[46:47], v[46:47], v[198:199]
	v_pk_mul_f32 v[42:43], v[42:43], v[202:203]
	v_pk_mul_f32 v[38:39], v[38:39], v[206:207]
	v_pk_mul_f32 v[34:35], v[34:35], v[210:211]
.Lnoresc2:
	s_waitcnt vmcnt(0) lgkmcnt(0)
	s_barrier
	s_cbranch_scc0 .LBB1_27

.LBB1_14:
	ds_read_b64_tr_b16 v[182:183], v169 offset:0
	ds_read_b64_tr_b16 v[184:185], v169 offset:0x800
	ds_read_b64_tr_b16 v[186:187], v169 offset:0x1000
	ds_read_b64_tr_b16 v[188:189], v169 offset:0x1800
	ds_read_b64_tr_b16 v[190:191], v169 offset:0x2000
	ds_read_b64_tr_b16 v[192:193], v169 offset:0x2800
	ds_read_b64_tr_b16 v[194:195], v169 offset:0x3000
	ds_read_b64_tr_b16 v[196:197], v169 offset:0x3800
	v_fmac_f32 v83, 0x3f800000, v1
	v_fmac_f32 v84, 0x40000000, v1
	v_fmac_f32 v85, 0x40400000, v1
	v_fmac_f32 v86, 0x41000000, v1
	v_fmac_f32 v87, 0x41100000, v1
	s_nop 0
	s_waitcnt lgkmcnt(0)
	v_fmac_f32 v88, 0x41200000, v1
	v_fmac_f32 v89, 0x41300000, v1
	v_fmac_f32 v90, 0x41800000, v1
	v_fmac_f32 v91, 0x41880000, v1
	v_fmac_f32 v92, 0x41900000, v1
	s_nop 0
	v_mfma_f32_32x32x16_f16 v[50:65], v[4:7], v[182:185], v[50:65]
	ds_read_b64_tr_b16 v[182:183], v169 offset:0x200
	ds_read_b64_tr_b16 v[184:185], v169 offset:0xa00
	v_fmac_f32 v93, 0x41980000, v1
	v_fmac_f32 v94, 0x41c00000, v1
	v_fmac_f32 v95, 0x41c80000, v1
	v_fmac_f32 v96, 0x41d00000, v1
	v_fmac_f32 v97, 0x41d80000, v1
	v_mfma_f32_32x32x16_f16 v[50:65], v[8:11], v[186:189], v[50:65]
	ds_read_b64_tr_b16 v[186:187], v169 offset:0x1200
	ds_read_b64_tr_b16 v[188:189], v169 offset:0x1a00
	v_fmac_f32 v98, 0x42000000, v1
	v_fmac_f32 v99, 0x42040000, v1
	v_fmac_f32 v100, 0x42080000, v1
	v_fmac_f32 v101, 0x420c0000, v1
	v_fmac_f32 v102, 0x42200000, v1
	v_mfma_f32_32x32x16_f16 v[50:65], v[12:15], v[190:193], v[50:65]
	ds_read_b64_tr_b16 v[190:191], v169 offset:0x2200
	ds_read_b64_tr_b16 v[192:193], v169 offset:0x2a00
	v_fmac_f32 v103, 0x42240000, v1
	v_fmac_f32 v104, 0x42280000, v1
	v_fmac_f32 v105, 0x422c0000, v1
	v_fmac_f32 v106, 0x42400000, v1
	v_fmac_f32 v107, 0x42440000, v1
	v_mfma_f32_32x32x16_f16 v[50:65], v[146:149], v[194:197], v[50:65]
	ds_read_b64_tr_b16 v[194:195], v169 offset:0x3200
	ds_read_b64_tr_b16 v[196:197], v169 offset:0x3a00
	v_fmac_f32 v108, 0x42480000, v1
	v_fmac_f32 v109, 0x424c0000, v1
	v_fmac_f32 v110, 0x42600000, v1
	v_fmac_f32 v111, 0x42640000, v1
	v_fmac_f32 v112, 0x42680000, v1
	s_nop 0
	s_waitcnt lgkmcnt(0)
	ds_read_b64_tr_b16 v[198:199], v169 offset:0x400
	ds_read_b64_tr_b16 v[200:201], v169 offset:0xc00
	ds_read_b64_tr_b16 v[202:203], v169 offset:0x1400
	ds_read_b64_tr_b16 v[204:205], v169 offset:0x1c00
	ds_read_b64_tr_b16 v[206:207], v169 offset:0x2400
	s_nop 0
	v_mfma_f32_32x32x16_f16 v[18:33], v[4:7], v[182:185], v[18:33]
	ds_read_b64_tr_b16 v[208:209], v169 offset:0x2c00
	ds_read_b64_tr_b16 v[184:185], v169 offset:0x3400
	v_cvt_f32_i32_e32 v183, v181
	v_max_f32_e32 v181, v83, v83
	v_max_f32_e32 v182, v82, v82
	v_max_f32_e32 v181, v182, v181
	v_max3_f32 v181, v181, v84, v85
	v_mfma_f32_32x32x16_f16 v[18:33], v[8:11], v[186:189], v[18:33]
	ds_read_b64_tr_b16 v[186:187], v169 offset:0x3c00
	v_max3_f32 v181, v181, v86, v87
	s_waitcnt lgkmcnt(0)
	ds_read_b64_tr_b16 v[210:211], v169 offset:0x600
	ds_read_b64_tr_b16 v[212:213], v169 offset:0xe00
	ds_read_b64_tr_b16 v[214:215], v169 offset:0x1600
	ds_read_b64_tr_b16 v[216:217], v169 offset:0x1e00
	ds_read_b64_tr_b16 v[188:189], v169 offset:0x2600
	v_mfma_f32_32x32x16_f16 v[18:33], v[12:15], v[190:193], v[18:33]
	ds_read_b64_tr_b16 v[190:191], v169 offset:0x2e00
	ds_read_b64_tr_b16 v[218:219], v169 offset:0x3600
	ds_read_b64_tr_b16 v[220:221], v169 offset:0x3e00
	v_max3_f32 v181, v181, v88, v89
	s_waitcnt lgkmcnt(0)
	v_fmac_f32 v113, 0x426c0000, v1
	v_mfma_f32_32x32x16_f16 v[66:81], v[4:7], v[198:201], v[66:81]
	v_mfma_f32_32x32x16_f16 v[34:49], v[4:7], v[210:213], v[34:49]
	v_max3_f32 v4, v181, v90, v91
	v_max3_f32 v4, v4, v92, v93
	v_max3_f32 v4, v4, v94, v95
	v_max3_f32 v4, v4, v96, v97
	v_max3_f32 v4, v4, v98, v99
	v_max3_f32 v4, v4, v100, v101
	v_max3_f32 v4, v4, v102, v103
	v_mfma_f32_32x32x16_f16 v[66:81], v[8:11], v[202:205], v[66:81]
	v_max3_f32 v4, v4, v104, v105
	v_max3_f32 v4, v4, v106, v107
	v_max3_f32 v4, v4, v108, v109
	v_max3_f32 v4, v4, v110, v111
	v_max3_f32 v4, v4, v112, v113
	v_fma_f32 v4, -v1, v183, v4
	v_mov_b32_e32 v5, v4
	v_mfma_f32_32x32x16_f16 v[34:49], v[8:11], v[214:217], v[34:49]
	s_nop 0
	v_permlane32_swap_b32_e32 v4, v5
	v_max3_f32 v182, v178, v4, v5
	v_sub_f32_e32 v4, v178, v182
	v_mul_f32_e32 v4, 0x3e0293ee, v4
	v_exp_f32_e32 v181, v4
	v_mfma_f32_32x32x16_f16 v[66:81], v[12:15], v[206:209], v[66:81]
	v_cmp_gt_f32_e32 vcc, 1.0, v181
	v_mfma_f32_32x32x16_f16 v[34:49], v[12:15], v[188:191], v[34:49]
	v_mfma_f32_32x32x16_f16 v[18:33], v[146:149], v[194:197], v[18:33]
	v_mfma_f32_32x32x16_f16 v[66:81], v[146:149], v[184:187], v[66:81]
	v_mfma_f32_32x32x16_f16 v[34:49], v[146:149], v[218:221], v[34:49]
	s_cbranch_vccz .LBB1_18
	s_and_saveexec_b64 s[4:5], s[2:3]
	ds_write_b32 v176, v181 offset:128
	s_or_b64 exec, exec, s[4:5]
	ds_read_b128 v[198:201], v177 offset:224
	ds_read_b128 v[202:205], v177 offset:192
	ds_read_b128 v[206:209], v177 offset:160
	ds_read_b128 v[210:213], v177 offset:128
.LBB1_18:
	v_mul_f32_e64 v4, -v1, v183
	v_sub_f32_e32 v4, v4, v182
	v_mul_f32_e32 v178, 0x3e0293ee, v4
	v_fmamk_f32 v4, v82, 0x3e0293ee, v178
	v_fmamk_f32 v5, v83, 0x3e0293ee, v178
	v_fmamk_f32 v6, v84, 0x3e0293ee, v178
	v_fmamk_f32 v7, v85, 0x3e0293ee, v178
	v_fmamk_f32 v8, v86, 0x3e0293ee, v178
	v_fmamk_f32 v9, v87, 0x3e0293ee, v178
	v_fmamk_f32 v10, v88, 0x3e0293ee, v178
	v_fmamk_f32 v11, v89, 0x3e0293ee, v178
	v_fmamk_f32 v12, v90, 0x3e0293ee, v178
	v_fmamk_f32 v13, v91, 0x3e0293ee, v178
	v_fmamk_f32 v14, v92, 0x3e0293ee, v178
	v_fmamk_f32 v15, v93, 0x3e0293ee, v178
	v_fmamk_f32 v82, v94, 0x3e0293ee, v178
	v_fmamk_f32 v83, v95, 0x3e0293ee, v178
	v_fmamk_f32 v84, v96, 0x3e0293ee, v178
	v_fmamk_f32 v85, v97, 0x3e0293ee, v178
	v_fmamk_f32 v192, v99, 0x3e0293ee, v178
	v_fmamk_f32 v193, v100, 0x3e0293ee, v178
	v_fmamk_f32 v183, v98, 0x3e0293ee, v178
	v_fmamk_f32 v218, v101, 0x3e0293ee, v178
	v_fmamk_f32 v219, v102, 0x3e0293ee, v178
	v_fmamk_f32 v220, v103, 0x3e0293ee, v178
	v_fmamk_f32 v221, v104, 0x3e0293ee, v178
	v_fmamk_f32 v222, v105, 0x3e0293ee, v178
	v_fmamk_f32 v223, v106, 0x3e0293ee, v178
	v_fmamk_f32 v224, v107, 0x3e0293ee, v178
	v_fmamk_f32 v225, v108, 0x3e0293ee, v178
	v_fmamk_f32 v226, v109, 0x3e0293ee, v178
	v_fmamk_f32 v227, v110, 0x3e0293ee, v178
	v_fmamk_f32 v228, v111, 0x3e0293ee, v178
	v_fmamk_f32 v229, v112, 0x3e0293ee, v178
	v_fmac_f32_e32 v178, 0x3e0293ee, v113
	v_exp_f32_e32 v230, v4
	v_exp_f32_e32 v231, v5
	v_exp_f32_e32 v232, v6
	v_exp_f32_e32 v233, v7
	v_exp_f32_e32 v234, v8
	v_exp_f32_e32 v235, v9
	v_exp_f32_e32 v236, v10
	v_exp_f32_e32 v237, v11
	v_exp_f32_e32 v238, v12
	v_exp_f32_e32 v239, v13
	v_exp_f32_e32 v240, v14
	v_exp_f32_e32 v241, v15
	v_exp_f32_e32 v242, v82
	v_exp_f32_e32 v243, v83
	v_exp_f32_e32 v244, v84
	v_exp_f32_e32 v245, v85
	s_cbranch_vccz .Lnoresc1
	s_waitcnt lgkmcnt(0)
	v_pk_mul_f32 v[64:65], v[64:65], v[200:201]
	v_pk_mul_f32 v[60:61], v[60:61], v[204:205]
	v_pk_mul_f32 v[56:57], v[56:57], v[208:209]
	v_pk_mul_f32 v[52:53], v[52:53], v[212:213]
	v_pk_mul_f32 v[62:63], v[62:63], v[198:199]
	v_pk_mul_f32 v[58:59], v[58:59], v[202:203]
	v_pk_mul_f32 v[54:55], v[54:55], v[206:207]
	v_pk_mul_f32 v[50:51], v[50:51], v[210:211]
	v_pk_mul_f32 v[32:33], v[32:33], v[200:201]
	v_pk_mul_f32 v[28:29], v[28:29], v[204:205]
	v_pk_mul_f32 v[24:25], v[24:25], v[208:209]
	v_pk_mul_f32 v[20:21], v[20:21], v[212:213]
	v_pk_mul_f32 v[30:31], v[30:31], v[198:199]
	v_pk_mul_f32 v[26:27], v[26:27], v[202:203]
	v_pk_mul_f32 v[22:23], v[22:23], v[206:207]
	v_pk_mul_f32 v[18:19], v[18:19], v[210:211]
	v_pk_mul_f32 v[80:81], v[80:81], v[200:201]
	v_pk_mul_f32 v[76:77], v[76:77], v[204:205]
	v_pk_mul_f32 v[72:73], v[72:73], v[208:209]
	v_pk_mul_f32 v[68:69], v[68:69], v[212:213]
	v_pk_mul_f32 v[78:79], v[78:79], v[198:199]
	v_pk_mul_f32 v[74:75], v[74:75], v[202:203]
	v_pk_mul_f32 v[70:71], v[70:71], v[206:207]
	v_pk_mul_f32 v[66:67], v[66:67], v[210:211]
	v_pk_mul_f32 v[48:49], v[48:49], v[200:201]
	v_pk_mul_f32 v[44:45], v[44:45], v[204:205]
	v_pk_mul_f32 v[40:41], v[40:41], v[208:209]
	v_pk_mul_f32 v[36:37], v[36:37], v[212:213]
	v_pk_mul_f32 v[46:47], v[46:47], v[198:199]
	v_pk_mul_f32 v[42:43], v[42:43], v[202:203]
	v_pk_mul_f32 v[38:39], v[38:39], v[206:207]
	v_pk_mul_f32 v[34:35], v[34:35], v[210:211]
.Lnoresc1:
	s_waitcnt vmcnt(0)
	s_barrier
	ds_read_b128 v[4:7], v172
	ds_read_b128 v[8:11], v172 offset:128
	v_exp_f32_e32 v183, v183
	v_exp_f32_e32 v246, v192
	v_exp_f32_e32 v247, v193
	s_waitcnt lgkmcnt(1)
	v_mfma_f32_32x32x16_f16 v[98:113], v[4:7], v[114:117], 0
	ds_read_b128 v[4:7], v172 offset:8192
	ds_read_b128 v[12:15], v172 offset:8320
	v_exp_f32_e32 v218, v218
	v_exp_f32_e32 v219, v219
	v_exp_f32_e32 v220, v220
	v_exp_f32_e32 v221, v221
	v_exp_f32_e32 v222, v222
	v_exp_f32_e32 v223, v223
	s_waitcnt lgkmcnt(1)
	v_mfma_f32_32x32x16_f16 v[82:97], v[4:7], v[114:117], 0
	ds_read_b128 v[4:7], v173
	ds_read_b128 v[146:149], v173 offset:8192
	ds_read_b128 v[184:187], v173 offset:128
	v_exp_f32_e32 v224, v224
	v_exp_f32_e32 v225, v225
	v_exp_f32_e32 v226, v226
	v_exp_f32_e32 v178, v178
	s_waitcnt lgkmcnt(2)
	v_mfma_f32_32x32x16_f16 v[98:113], v[4:7], v[118:121], v[98:113]
	ds_read_b128 v[188:191], v173 offset:8320
	ds_read_b128 v[4:7], v174
	ds_read_b128 v[194:197], v174 offset:128
	ds_read_b128 v[198:201], v174 offset:8192
	ds_read_b128 v[202:205], v174 offset:8320
	ds_read_b128 v[206:209], v175
	ds_read_b128 v[210:213], v175 offset:128
	s_waitcnt lgkmcnt(8)
	v_mfma_f32_32x32x16_f16 v[82:97], v[146:149], v[118:121], v[82:97]
	ds_read_b128 v[146:149], v175 offset:8192
	ds_read_b128 v[214:217], v175 offset:8320
	s_waitcnt lgkmcnt(7)
	v_mfma_f32_32x32x16_f16 v[98:113], v[4:7], v[122:125], v[98:113]
	v_add_f32_e32 v4, 0, v230
	v_add_f32_e32 v4, v231, v4
	v_add_f32_e32 v4, v232, v4
	v_add_f32_e32 v4, v233, v4
	v_add_f32_e32 v4, v234, v4
	v_add_f32_e32 v4, v235, v4
	v_add_f32_e32 v4, v236, v4
	s_waitcnt lgkmcnt(5)
	v_mfma_f32_32x32x16_f16 v[82:97], v[198:201], v[122:125], v[82:97]
	v_add_f32_e32 v4, v237, v4
	v_add_f32_e32 v4, v238, v4
	v_add_f32_e32 v4, v239, v4
	v_add_f32_e32 v4, v240, v4
	v_add_f32_e32 v4, v241, v4
	v_add_f32_e32 v4, v242, v4
	v_add_f32_e32 v4, v243, v4
	s_waitcnt lgkmcnt(3)
	v_mfma_f32_32x32x16_f16 v[98:113], v[206:209], v[126:129], v[98:113]
	v_add_f32_e32 v4, v244, v4
	v_add_f32_e32 v4, v245, v4
	v_add_f32_e32 v4, v183, v4
	v_add_f32_e32 v4, v246, v4
	v_add_f32_e32 v4, v247, v4
	v_add_f32_e32 v4, v218, v4
	v_add_f32_e32 v4, v219, v4
	s_waitcnt lgkmcnt(1)
	v_mfma_f32_32x32x16_f16 v[82:97], v[146:149], v[126:129], v[82:97]
	v_add_f32_e32 v4, v220, v4
	v_add_f32_e32 v4, v221, v4
	v_add_f32_e32 v4, v222, v4
	v_exp_f32_e32 v198, v227
	v_add_f32_e32 v4, v223, v4
	v_exp_f32_e32 v199, v228
	v_add_f32_e32 v4, v224, v4
	v_mfma_f32_32x32x16_f16 v[98:113], v[8:11], v[130:133], v[98:113]
	v_exp_f32_e32 v200, v229
	v_add_f32_e32 v4, v225, v4
	v_add_f32_e32 v4, v226, v4
	v_add_f32_e32 v4, v198, v4
	v_add_f32_e32 v4, v199, v4
	v_add_f32_e32 v4, v200, v4
	v_add_f32_e32 v192, v178, v4
	v_mfma_f32_32x32x16_f16 v[82:97], v[12:15], v[130:133], v[82:97]
	v_mov_b32_e32 v193, v192
	v_cvt_pk_f16_f32 v4, v230, v231
	v_cvt_pk_f16_f32 v5, v232, v233
	v_cvt_pk_f16_f32 v6, v234, v235
	v_cvt_pk_f16_f32 v7, v236, v237
	v_cvt_pk_f16_f32 v8, v238, v239
	v_cvt_pk_f16_f32 v9, v240, v241
	v_mfma_f32_32x32x16_f16 v[98:113], v[184:187], v[134:137], v[98:113]
	v_cvt_pk_f16_f32 v10, v242, v243
	v_cvt_pk_f16_f32 v11, v244, v245
	v_cvt_pk_f16_f32 v12, v183, v246
	v_cvt_pk_f16_f32 v13, v247, v218
	v_cvt_pk_f16_f32 v14, v219, v220
	v_cvt_pk_f16_f32 v15, v221, v222
	v_cvt_pk_f16_f32 v146, v223, v224
	v_mfma_f32_32x32x16_f16 v[82:97], v[188:191], v[134:137], v[82:97]
	v_cvt_pk_f16_f32 v147, v225, v226
	v_cvt_pk_f16_f32 v148, v198, v199
	v_cvt_pk_f16_f32 v149, v200, v178
	v_permlane32_swap_b32_e32 v192, v193
	v_permlane32_swap_b32_e32 v4, v6
	v_mfma_f32_32x32x16_f16 v[98:113], v[194:197], v[138:141], v[98:113]
	v_permlane32_swap_b32_e32 v5, v7
	v_permlane32_swap_b32_e32 v8, v10
	v_permlane32_swap_b32_e32 v9, v11
	v_permlane32_swap_b32_e32 v12, v14
	v_mfma_f32_32x32x16_f16 v[82:97], v[202:205], v[138:141], v[82:97]
	v_permlane32_swap_b32_e32 v13, v15
	v_permlane32_swap_b32_e32 v146, v148
	v_permlane32_swap_b32_e32 v147, v149
	v_mfma_f32_32x32x16_f16 v[98:113], v[210:213], v[142:145], v[98:113]
	s_waitcnt lgkmcnt(0)
	v_mfma_f32_32x32x16_f16 v[82:97], v[214:217], v[142:145], v[82:97]
	s_add_i32 s72, s72, 2
	s_cmp_gt_u32 s72, s83
	s_cbranch_scc1 .LBB1_20
	s_add_u32 s4, s74, 0x18000
	s_addc_u32 s5, s75, 0
	s_add_i32 m0, s69, 0x18000
	s_nop 0
	global_load_lds_dwordx4 v154, s[4:5]
	s_add_i32 m0, s69, 0x1a000
	s_nop 0
	global_load_lds_dwordx4 v250, s[4:5]
	s_add_i32 m0, s69, 0x1c000
	s_nop 0
	global_load_lds_dwordx4 v251, s[4:5]
	s_add_i32 m0, s69, 0x1e000
	s_nop 0
	global_load_lds_dwordx4 v252, s[4:5]
